# speedup vs baseline: 1.0998x; 1.0012x over previous
.LBB1_55:
	s_or_b64 exec, exec, s[2:3]
	v_and_b32_e32 v110, 63, v175
	v_lshrrev_b32_e32 v111, 6, v175
	v_lshlrev_b32_e32 v111, 4, v111
	s_movk_i32 s10, 0x556
	v_mov_b32_e32 v119, v110
	v_mul_u32_u24_e32 v112, s10, v119
	v_lshrrev_b32_e32 v112, 16, v112
	v_mul_u32_u24_e32 v113, 48, v112
	v_sub_u32_e32 v113, v119, v113
	v_add_u32_e32 v114, v111, v112
	v_mul_u32_u24_e32 v156, 0x300, v114
	v_lshl_add_u32 v156, v113, 4, v156
	v_xor_b32_e32 v159, 64, v156
	v_add_u32_e32 v115, v174, v114
	v_mul_u32_u24_e32 v115, 0x300, v115
	v_add_u32_e32 v115, v115, v118
	v_lshl_add_u32 v115, v113, 2, v115
	v_lshlrev_b32_e32 v162, 2, v115
	v_lshlrev_b32_e32 v165, 1, v115
	v_lshl_add_u32 v116, v113, 2, v118
	v_lshlrev_b32_e32 v116, 2, v116
	global_load_dwordx4 v[144:147], v116, s[50:51]
	v_add_u32_e32 v119, 64, v110
	v_mul_u32_u24_e32 v112, s10, v119
	v_lshrrev_b32_e32 v112, 16, v112
	v_mul_u32_u24_e32 v113, 48, v112
	v_sub_u32_e32 v113, v119, v113
	v_add_u32_e32 v114, v111, v112
	v_mul_u32_u24_e32 v157, 0x300, v114
	v_lshl_add_u32 v157, v113, 4, v157
	v_xor_b32_e32 v160, 64, v157
	v_add_u32_e32 v115, v174, v114
	v_mul_u32_u24_e32 v115, 0x300, v115
	v_add_u32_e32 v115, v115, v118
	v_lshl_add_u32 v115, v113, 2, v115
	v_lshlrev_b32_e32 v163, 2, v115
	v_lshlrev_b32_e32 v166, 1, v115
	v_lshl_add_u32 v116, v113, 2, v118
	v_lshlrev_b32_e32 v116, 2, v116
	global_load_dwordx4 v[148:151], v116, s[50:51]
	v_add_u32_e32 v119, 128, v110
	v_mul_u32_u24_e32 v112, s10, v119
	v_lshrrev_b32_e32 v112, 16, v112
	v_mul_u32_u24_e32 v113, 48, v112
	v_sub_u32_e32 v113, v119, v113
	v_add_u32_e32 v114, v111, v112
	v_mul_u32_u24_e32 v158, 0x300, v114
	v_lshl_add_u32 v158, v113, 4, v158
	v_xor_b32_e32 v161, 64, v158
	v_add_u32_e32 v115, v174, v114
	v_mul_u32_u24_e32 v115, 0x300, v115
	v_add_u32_e32 v115, v115, v118
	v_lshl_add_u32 v115, v113, 2, v115
	v_lshlrev_b32_e32 v164, 2, v115
	v_lshlrev_b32_e32 v167, 1, v115
	v_lshl_add_u32 v116, v113, 2, v118
	v_lshlrev_b32_e32 v116, 2, v116
	global_load_dwordx4 v[152:155], v116, s[50:51]
	global_load_dwordx2 v[120:121], v165, s[38:39] nt
	global_load_dwordx2 v[122:123], v166, s[38:39] nt
	global_load_dwordx2 v[124:125], v167, s[38:39] nt
	v_add_u32_e32 v117, 0x1800, v165
	global_load_dwordx2 v[126:127], v117, s[38:39] nt
	v_add_u32_e32 v117, 0x1800, v166
	global_load_dwordx2 v[128:129], v117, s[38:39] nt
	v_add_u32_e32 v117, 0x1800, v167
	global_load_dwordx2 v[130:131], v117, s[38:39] nt
	v_add_u32_e32 v117, 0x3000, v165
	global_load_dwordx2 v[132:133], v117, s[38:39] nt
	v_add_u32_e32 v117, 0x3000, v166
	global_load_dwordx2 v[134:135], v117, s[38:39] nt
	v_add_u32_e32 v117, 0x3000, v167
	global_load_dwordx2 v[136:137], v117, s[38:39] nt
	v_add_u32_e32 v117, 0x4800, v165
	global_load_dwordx2 v[138:139], v117, s[38:39] nt
	v_add_u32_e32 v117, 0x4800, v166
	global_load_dwordx2 v[140:141], v117, s[38:39] nt
	v_add_u32_e32 v117, 0x4800, v167
	global_load_dwordx2 v[142:143], v117, s[38:39] nt
	v_add_u32_e32 v117, 0x30000, v165
	global_load_dwordx2 v[232:233], v117, s[38:39] nt
	v_add_u32_e32 v117, 0x30000, v166
	global_load_dwordx2 v[234:235], v117, s[38:39] nt
	v_add_u32_e32 v117, 0x30000, v167
	global_load_dwordx2 v[236:237], v117, s[38:39] nt
	v_add_u32_e32 v117, 0x31800, v165
	global_load_dwordx2 v[238:239], v117, s[38:39] nt
	v_add_u32_e32 v117, 0x31800, v166
	global_load_dwordx2 v[240:241], v117, s[38:39] nt
	v_add_u32_e32 v117, 0x31800, v167
	global_load_dwordx2 v[242:243], v117, s[38:39] nt
	v_add_u32_e32 v117, 0x33000, v165
	global_load_dwordx2 v[244:245], v117, s[38:39] nt
	v_add_u32_e32 v117, 0x33000, v166
	global_load_dwordx2 v[246:247], v117, s[38:39] nt
	v_add_u32_e32 v117, 0x33000, v167
	global_load_dwordx2 v[248:249], v117, s[38:39] nt
	v_add_u32_e32 v117, 0x34800, v165
	global_load_dwordx2 v[250:251], v117, s[38:39] nt
	v_add_u32_e32 v117, 0x34800, v166
	global_load_dwordx2 v[252:253], v117, s[38:39] nt
	v_add_u32_e32 v117, 0x34800, v167
	global_load_dwordx2 v[254:255], v117, s[38:39] nt
	s_barrier
	v_and_b32_e32 v205, 16, v175
	v_lshrrev_b32_e32 v207, 2, v175
	v_or_b32_e32 v206, v179, v177
	v_and_or_b32 v180, v207, 12, v180
	v_bitop3_b32 v177, v179, v205, v177 bitop3:0x36
	v_lshlrev_b32_e32 v177, 2, v177
	v_mul_lo_u32 v179, v180, s67
	v_add3_u32 v177, 0, v177, v179
	ds_write2st64_b32 v177, v58, v59 offset1:3
	ds_write2st64_b32 v177, v60, v61 offset0:6 offset1:9
	ds_write2st64_b32 v177, v102, v103 offset0:48 offset1:51
	ds_write2st64_b32 v177, v104, v105 offset0:54 offset1:57
	v_add_u32_e32 v58, 16, v206
	v_bitop3_b32 v58, v58, v175, 16 bitop3:0x78
	v_lshlrev_b32_e32 v58, 2, v58
	v_add3_u32 v102, 0, v58, v179
	ds_write2st64_b32 v102, v78, v79 offset1:3
	v_add_u32_e32 v78, 32, v206
	v_bitop3_b32 v78, v78, v175, 16 bitop3:0x78
	v_lshlrev_b32_e32 v78, 2, v78
	v_add3_u32 v103, 0, v78, v179
	ds_write2st64_b32 v102, v80, v81 offset0:6 offset1:9
	ds_write2st64_b32 v102, v86, v87 offset0:48 offset1:51
	ds_write2st64_b32 v102, v88, v89 offset0:54 offset1:57
	ds_write2st64_b32 v103, v62, v63 offset1:3
	ds_write2st64_b32 v103, v64, v65 offset0:6 offset1:9
	ds_write2st64_b32 v103, v70, v71 offset0:48 offset1:51
	ds_write2st64_b32 v103, v72, v73 offset0:54 offset1:57
	v_add_u32_e32 v62, 0x60, v206
	v_bitop3_b32 v62, v62, v175, 16 bitop3:0x78
	v_lshlrev_b32_e32 v62, 2, v62
	v_add3_u32 v104, 0, v62, v179
	v_add_u32_e32 v62, 0x70, v206
	v_bitop3_b32 v62, v62, v175, 16 bitop3:0x78
	v_lshlrev_b32_e32 v62, 2, v62
	s_movk_i32 s2, 0x80
	ds_write2st64_b32 v104, v94, v95 offset1:3
	ds_write2st64_b32 v104, v96, v97 offset0:6 offset1:9
	ds_write2st64_b32 v104, v98, v99 offset0:48 offset1:51
	ds_write2st64_b32 v104, v100, v101 offset0:54 offset1:57
	v_add3_u32 v101, 0, v62, v179
	v_bitop3_b32 v62, v206, v205, s2 bitop3:0x36
	v_lshlrev_b32_e32 v62, 2, v62
	v_add3_u32 v105, 0, v62, v179
	ds_write2st64_b32 v101, v82, v83 offset1:3
	ds_write2st64_b32 v101, v84, v85 offset0:6 offset1:9
	ds_write2st64_b32 v101, v90, v91 offset0:48 offset1:51
	ds_write2st64_b32 v101, v92, v93 offset0:54 offset1:57
	ds_write2st64_b32 v105, v66, v67 offset1:3
	ds_write2st64_b32 v105, v68, v69 offset0:6 offset1:9
	ds_write2st64_b32 v105, v74, v75 offset0:48 offset1:51
	ds_write2st64_b32 v105, v76, v77 offset0:54 offset1:57
	s_waitcnt lgkmcnt(0)
	s_barrier
	ds_read_b128 v[182:185], v156
	ds_read_b128 v[186:189], v157
	ds_read_b128 v[190:193], v158
	ds_read_b128 v[194:197], v159 offset:3072
	ds_read_b128 v[198:201], v160 offset:3072
	ds_read_b128 v[202:205], v161 offset:3072
	ds_read_b128 v[206:209], v156 offset:6144
	ds_read_b128 v[210:213], v157 offset:6144
	ds_read_b128 v[214:217], v158 offset:6144
	ds_read_b128 v[218:221], v159 offset:9216
	ds_read_b128 v[222:225], v160 offset:9216
	ds_read_b128 v[226:229], v161 offset:9216
	s_waitcnt vmcnt(12)
	v_cvt_f32_f16_e32 v112, v120
	v_cvt_f32_f16_sdwa v113, v120 dst_sel:DWORD dst_unused:UNUSED_PAD src0_sel:WORD_1
	v_cvt_f32_f16_e32 v114, v121
	v_cvt_f32_f16_sdwa v115, v121 dst_sel:DWORD dst_unused:UNUSED_PAD src0_sel:WORD_1
	s_waitcnt lgkmcnt(11)
	v_pk_fma_f32 v[182:183], v[112:113], v[144:145], v[182:183]
	v_pk_fma_f32 v[184:185], v[114:115], v[146:147], v[184:185]
	global_store_dwordx4 v162, v[182:185], s[46:47] nt
	v_cvt_f32_f16_e32 v112, v122
	v_cvt_f32_f16_sdwa v113, v122 dst_sel:DWORD dst_unused:UNUSED_PAD src0_sel:WORD_1
	v_cvt_f32_f16_e32 v114, v123
	v_cvt_f32_f16_sdwa v115, v123 dst_sel:DWORD dst_unused:UNUSED_PAD src0_sel:WORD_1
	s_waitcnt lgkmcnt(10)
	v_pk_fma_f32 v[186:187], v[112:113], v[148:149], v[186:187]
	v_pk_fma_f32 v[188:189], v[114:115], v[150:151], v[188:189]
	global_store_dwordx4 v163, v[186:189], s[46:47] nt
	v_cvt_f32_f16_e32 v112, v124
	v_cvt_f32_f16_sdwa v113, v124 dst_sel:DWORD dst_unused:UNUSED_PAD src0_sel:WORD_1
	v_cvt_f32_f16_e32 v114, v125
	v_cvt_f32_f16_sdwa v115, v125 dst_sel:DWORD dst_unused:UNUSED_PAD src0_sel:WORD_1
	s_waitcnt lgkmcnt(9)
	v_pk_fma_f32 v[190:191], v[112:113], v[152:153], v[190:191]
	v_pk_fma_f32 v[192:193], v[114:115], v[154:155], v[192:193]
	global_store_dwordx4 v164, v[190:193], s[46:47] nt
	v_cvt_f32_f16_e32 v112, v126
	v_cvt_f32_f16_sdwa v113, v126 dst_sel:DWORD dst_unused:UNUSED_PAD src0_sel:WORD_1
	v_cvt_f32_f16_e32 v114, v127
	v_cvt_f32_f16_sdwa v115, v127 dst_sel:DWORD dst_unused:UNUSED_PAD src0_sel:WORD_1
	v_add_u32_e32 v117, 0x3000, v162
	s_waitcnt lgkmcnt(8)
	v_pk_fma_f32 v[194:195], v[112:113], v[144:145], v[194:195]
	v_pk_fma_f32 v[196:197], v[114:115], v[146:147], v[196:197]
	global_store_dwordx4 v117, v[194:197], s[46:47] nt
	v_cvt_f32_f16_e32 v112, v128
	v_cvt_f32_f16_sdwa v113, v128 dst_sel:DWORD dst_unused:UNUSED_PAD src0_sel:WORD_1
	v_cvt_f32_f16_e32 v114, v129
	v_cvt_f32_f16_sdwa v115, v129 dst_sel:DWORD dst_unused:UNUSED_PAD src0_sel:WORD_1
	v_add_u32_e32 v117, 0x3000, v163
	s_waitcnt lgkmcnt(7)
	v_pk_fma_f32 v[198:199], v[112:113], v[148:149], v[198:199]
	v_pk_fma_f32 v[200:201], v[114:115], v[150:151], v[200:201]
	global_store_dwordx4 v117, v[198:201], s[46:47] nt
	v_cvt_f32_f16_e32 v112, v130
	v_cvt_f32_f16_sdwa v113, v130 dst_sel:DWORD dst_unused:UNUSED_PAD src0_sel:WORD_1
	v_cvt_f32_f16_e32 v114, v131
	v_cvt_f32_f16_sdwa v115, v131 dst_sel:DWORD dst_unused:UNUSED_PAD src0_sel:WORD_1
	v_add_u32_e32 v117, 0x3000, v164
	s_waitcnt lgkmcnt(6)
	v_pk_fma_f32 v[202:203], v[112:113], v[152:153], v[202:203]
	v_pk_fma_f32 v[204:205], v[114:115], v[154:155], v[204:205]
	global_store_dwordx4 v117, v[202:205], s[46:47] nt
	v_cvt_f32_f16_e32 v112, v132
	v_cvt_f32_f16_sdwa v113, v132 dst_sel:DWORD dst_unused:UNUSED_PAD src0_sel:WORD_1
	v_cvt_f32_f16_e32 v114, v133
	v_cvt_f32_f16_sdwa v115, v133 dst_sel:DWORD dst_unused:UNUSED_PAD src0_sel:WORD_1
	v_add_u32_e32 v117, 0x6000, v162
	s_waitcnt lgkmcnt(5)
	v_pk_fma_f32 v[206:207], v[112:113], v[144:145], v[206:207]
	v_pk_fma_f32 v[208:209], v[114:115], v[146:147], v[208:209]
	global_store_dwordx4 v117, v[206:209], s[46:47] nt
	v_cvt_f32_f16_e32 v112, v134
	v_cvt_f32_f16_sdwa v113, v134 dst_sel:DWORD dst_unused:UNUSED_PAD src0_sel:WORD_1
	v_cvt_f32_f16_e32 v114, v135
	v_cvt_f32_f16_sdwa v115, v135 dst_sel:DWORD dst_unused:UNUSED_PAD src0_sel:WORD_1
	v_add_u32_e32 v117, 0x6000, v163
	s_waitcnt lgkmcnt(4)
	v_pk_fma_f32 v[210:211], v[112:113], v[148:149], v[210:211]
	v_pk_fma_f32 v[212:213], v[114:115], v[150:151], v[212:213]
	global_store_dwordx4 v117, v[210:213], s[46:47] nt
	v_cvt_f32_f16_e32 v112, v136
	v_cvt_f32_f16_sdwa v113, v136 dst_sel:DWORD dst_unused:UNUSED_PAD src0_sel:WORD_1
	v_cvt_f32_f16_e32 v114, v137
	v_cvt_f32_f16_sdwa v115, v137 dst_sel:DWORD dst_unused:UNUSED_PAD src0_sel:WORD_1
	v_add_u32_e32 v117, 0x6000, v164
	s_waitcnt lgkmcnt(3)
	v_pk_fma_f32 v[214:215], v[112:113], v[152:153], v[214:215]
	v_pk_fma_f32 v[216:217], v[114:115], v[154:155], v[216:217]
	global_store_dwordx4 v117, v[214:217], s[46:47] nt
	v_cvt_f32_f16_e32 v112, v138
	v_cvt_f32_f16_sdwa v113, v138 dst_sel:DWORD dst_unused:UNUSED_PAD src0_sel:WORD_1
	v_cvt_f32_f16_e32 v114, v139
	v_cvt_f32_f16_sdwa v115, v139 dst_sel:DWORD dst_unused:UNUSED_PAD src0_sel:WORD_1
	v_add_u32_e32 v117, 0x9000, v162
	s_waitcnt lgkmcnt(2)
	v_pk_fma_f32 v[218:219], v[112:113], v[144:145], v[218:219]
	v_pk_fma_f32 v[220:221], v[114:115], v[146:147], v[220:221]
	global_store_dwordx4 v117, v[218:221], s[46:47] nt
	v_cvt_f32_f16_e32 v112, v140
	v_cvt_f32_f16_sdwa v113, v140 dst_sel:DWORD dst_unused:UNUSED_PAD src0_sel:WORD_1
	v_cvt_f32_f16_e32 v114, v141
	v_cvt_f32_f16_sdwa v115, v141 dst_sel:DWORD dst_unused:UNUSED_PAD src0_sel:WORD_1
	v_add_u32_e32 v117, 0x9000, v163
	s_waitcnt lgkmcnt(1)
	v_pk_fma_f32 v[222:223], v[112:113], v[148:149], v[222:223]
	v_pk_fma_f32 v[224:225], v[114:115], v[150:151], v[224:225]
	global_store_dwordx4 v117, v[222:225], s[46:47] nt
	v_cvt_f32_f16_e32 v112, v142
	v_cvt_f32_f16_sdwa v113, v142 dst_sel:DWORD dst_unused:UNUSED_PAD src0_sel:WORD_1
	v_cvt_f32_f16_e32 v114, v143
	v_cvt_f32_f16_sdwa v115, v143 dst_sel:DWORD dst_unused:UNUSED_PAD src0_sel:WORD_1
	v_add_u32_e32 v117, 0x9000, v164
	s_waitcnt lgkmcnt(0)
	v_pk_fma_f32 v[226:227], v[112:113], v[152:153], v[226:227]
	v_pk_fma_f32 v[228:229], v[114:115], v[154:155], v[228:229]
	global_store_dwordx4 v117, v[226:229], s[46:47] nt
	s_barrier
	ds_write2st64_b32 v177, v14, v15 offset1:3
	ds_write2st64_b32 v177, v16, v17 offset0:6 offset1:9
	ds_write2st64_b32 v177, v38, v39 offset0:48 offset1:51
	ds_write2st64_b32 v177, v40, v41 offset0:54 offset1:57
	ds_write2st64_b32 v102, v6, v7 offset1:3
	ds_write2st64_b32 v102, v8, v9 offset0:6 offset1:9
	ds_write2st64_b32 v102, v26, v27 offset0:48 offset1:51
	ds_write2st64_b32 v102, v28, v29 offset0:54 offset1:57
	ds_write2st64_b32 v103, v2, v3 offset1:3
	ds_write2st64_b32 v103, v4, v5 offset0:6 offset1:9
	ds_write2st64_b32 v103, v18, v19 offset0:48 offset1:51
	ds_write2st64_b32 v103, v20, v21 offset0:54 offset1:57
	ds_write2st64_b32 v104, v30, v31 offset1:3
	ds_write2st64_b32 v104, v32, v33 offset0:6 offset1:9
	ds_write2st64_b32 v104, v46, v47 offset0:48 offset1:51
	ds_write2st64_b32 v104, v48, v49 offset0:54 offset1:57
	ds_write2st64_b32 v101, v22, v23 offset1:3
	ds_write2st64_b32 v101, v24, v25 offset0:6 offset1:9
	ds_write2st64_b32 v101, v42, v43 offset0:48 offset1:51
	ds_write2st64_b32 v101, v44, v45 offset0:54 offset1:57
	ds_write2st64_b32 v105, v10, v11 offset1:3
	ds_write2st64_b32 v105, v12, v13 offset0:6 offset1:9
	ds_write2st64_b32 v105, v34, v35 offset0:48 offset1:51
	ds_write2st64_b32 v105, v36, v37 offset0:54 offset1:57
	s_waitcnt lgkmcnt(0)
	s_barrier
	s_and_saveexec_b64 s[100:101], s[34:35]
	s_cbranch_execz .Lpf_skip_g2
	v_readfirstlane_b32 s10, v173
	s_lshl_b32 s10, s10, 7
	s_add_u32 s10, s64, s10
	s_addc_u32 s11, s65, 0
	global_atomic_add v231, v109, v1, s[10:11] sc0

.Lpf_end_g2:
	ds_read_b128 v[182:185], v156
	ds_read_b128 v[186:189], v157
	ds_read_b128 v[190:193], v158
	ds_read_b128 v[194:197], v159 offset:3072
	ds_read_b128 v[198:201], v160 offset:3072
	ds_read_b128 v[202:205], v161 offset:3072
	ds_read_b128 v[206:209], v156 offset:6144
	ds_read_b128 v[210:213], v157 offset:6144
	ds_read_b128 v[214:217], v158 offset:6144
	ds_read_b128 v[218:221], v159 offset:9216
	ds_read_b128 v[222:225], v160 offset:9216
	ds_read_b128 v[226:229], v161 offset:9216
	s_waitcnt vmcnt(12)
	v_cvt_f32_f16_e32 v112, v232
	v_cvt_f32_f16_sdwa v113, v232 dst_sel:DWORD dst_unused:UNUSED_PAD src0_sel:WORD_1
	v_cvt_f32_f16_e32 v114, v233
	v_cvt_f32_f16_sdwa v115, v233 dst_sel:DWORD dst_unused:UNUSED_PAD src0_sel:WORD_1
	v_add_u32_e32 v117, 0x60000, v162
	s_waitcnt lgkmcnt(11)
	v_pk_fma_f32 v[182:183], v[112:113], v[144:145], v[182:183]
	v_pk_fma_f32 v[184:185], v[114:115], v[146:147], v[184:185]
	global_store_dwordx4 v117, v[182:185], s[46:47] nt
	v_cvt_f32_f16_e32 v112, v234
	v_cvt_f32_f16_sdwa v113, v234 dst_sel:DWORD dst_unused:UNUSED_PAD src0_sel:WORD_1
	v_cvt_f32_f16_e32 v114, v235
	v_cvt_f32_f16_sdwa v115, v235 dst_sel:DWORD dst_unused:UNUSED_PAD src0_sel:WORD_1
	v_add_u32_e32 v117, 0x60000, v163
	s_waitcnt lgkmcnt(10)
	v_pk_fma_f32 v[186:187], v[112:113], v[148:149], v[186:187]
	v_pk_fma_f32 v[188:189], v[114:115], v[150:151], v[188:189]
	global_store_dwordx4 v117, v[186:189], s[46:47] nt
	v_cvt_f32_f16_e32 v112, v236
	v_cvt_f32_f16_sdwa v113, v236 dst_sel:DWORD dst_unused:UNUSED_PAD src0_sel:WORD_1
	v_cvt_f32_f16_e32 v114, v237
	v_cvt_f32_f16_sdwa v115, v237 dst_sel:DWORD dst_unused:UNUSED_PAD src0_sel:WORD_1
	v_add_u32_e32 v117, 0x60000, v164
	s_waitcnt lgkmcnt(9)
	v_pk_fma_f32 v[190:191], v[112:113], v[152:153], v[190:191]
	v_pk_fma_f32 v[192:193], v[114:115], v[154:155], v[192:193]
	global_store_dwordx4 v117, v[190:193], s[46:47] nt
	v_cvt_f32_f16_e32 v112, v238
	v_cvt_f32_f16_sdwa v113, v238 dst_sel:DWORD dst_unused:UNUSED_PAD src0_sel:WORD_1
	v_cvt_f32_f16_e32 v114, v239
	v_cvt_f32_f16_sdwa v115, v239 dst_sel:DWORD dst_unused:UNUSED_PAD src0_sel:WORD_1
	v_add_u32_e32 v117, 0x63000, v162
	s_waitcnt lgkmcnt(8)
	v_pk_fma_f32 v[194:195], v[112:113], v[144:145], v[194:195]
	v_pk_fma_f32 v[196:197], v[114:115], v[146:147], v[196:197]
	global_store_dwordx4 v117, v[194:197], s[46:47] nt
	v_cvt_f32_f16_e32 v112, v240
	v_cvt_f32_f16_sdwa v113, v240 dst_sel:DWORD dst_unused:UNUSED_PAD src0_sel:WORD_1
	v_cvt_f32_f16_e32 v114, v241
	v_cvt_f32_f16_sdwa v115, v241 dst_sel:DWORD dst_unused:UNUSED_PAD src0_sel:WORD_1
	v_add_u32_e32 v117, 0x63000, v163
	s_waitcnt lgkmcnt(7)
	v_pk_fma_f32 v[198:199], v[112:113], v[148:149], v[198:199]
	v_pk_fma_f32 v[200:201], v[114:115], v[150:151], v[200:201]
	global_store_dwordx4 v117, v[198:201], s[46:47] nt
	v_cvt_f32_f16_e32 v112, v242
	v_cvt_f32_f16_sdwa v113, v242 dst_sel:DWORD dst_unused:UNUSED_PAD src0_sel:WORD_1
	v_cvt_f32_f16_e32 v114, v243
	v_cvt_f32_f16_sdwa v115, v243 dst_sel:DWORD dst_unused:UNUSED_PAD src0_sel:WORD_1
	v_add_u32_e32 v117, 0x63000, v164
	s_waitcnt lgkmcnt(6)
	v_pk_fma_f32 v[202:203], v[112:113], v[152:153], v[202:203]
	v_pk_fma_f32 v[204:205], v[114:115], v[154:155], v[204:205]
	global_store_dwordx4 v117, v[202:205], s[46:47] nt
	v_cvt_f32_f16_e32 v112, v244
	v_cvt_f32_f16_sdwa v113, v244 dst_sel:DWORD dst_unused:UNUSED_PAD src0_sel:WORD_1
	v_cvt_f32_f16_e32 v114, v245
	v_cvt_f32_f16_sdwa v115, v245 dst_sel:DWORD dst_unused:UNUSED_PAD src0_sel:WORD_1
	v_add_u32_e32 v117, 0x66000, v162
	s_waitcnt lgkmcnt(5)
	v_pk_fma_f32 v[206:207], v[112:113], v[144:145], v[206:207]
	v_pk_fma_f32 v[208:209], v[114:115], v[146:147], v[208:209]
	global_store_dwordx4 v117, v[206:209], s[46:47] nt
	v_cvt_f32_f16_e32 v112, v246
	v_cvt_f32_f16_sdwa v113, v246 dst_sel:DWORD dst_unused:UNUSED_PAD src0_sel:WORD_1
	v_cvt_f32_f16_e32 v114, v247
	v_cvt_f32_f16_sdwa v115, v247 dst_sel:DWORD dst_unused:UNUSED_PAD src0_sel:WORD_1
	v_add_u32_e32 v117, 0x66000, v163
	s_waitcnt lgkmcnt(4)
	v_pk_fma_f32 v[210:211], v[112:113], v[148:149], v[210:211]
	v_pk_fma_f32 v[212:213], v[114:115], v[150:151], v[212:213]
	global_store_dwordx4 v117, v[210:213], s[46:47] nt
	v_cvt_f32_f16_e32 v112, v248
	v_cvt_f32_f16_sdwa v113, v248 dst_sel:DWORD dst_unused:UNUSED_PAD src0_sel:WORD_1
	v_cvt_f32_f16_e32 v114, v249
	v_cvt_f32_f16_sdwa v115, v249 dst_sel:DWORD dst_unused:UNUSED_PAD src0_sel:WORD_1
	v_add_u32_e32 v117, 0x66000, v164
	s_waitcnt lgkmcnt(3)
	v_pk_fma_f32 v[214:215], v[112:113], v[152:153], v[214:215]
	v_pk_fma_f32 v[216:217], v[114:115], v[154:155], v[216:217]
	global_store_dwordx4 v117, v[214:217], s[46:47] nt
	v_cvt_f32_f16_e32 v112, v250
	v_cvt_f32_f16_sdwa v113, v250 dst_sel:DWORD dst_unused:UNUSED_PAD src0_sel:WORD_1
	v_cvt_f32_f16_e32 v114, v251
	v_cvt_f32_f16_sdwa v115, v251 dst_sel:DWORD dst_unused:UNUSED_PAD src0_sel:WORD_1
	v_add_u32_e32 v117, 0x69000, v162
	s_waitcnt lgkmcnt(2)
	v_pk_fma_f32 v[218:219], v[112:113], v[144:145], v[218:219]
	v_pk_fma_f32 v[220:221], v[114:115], v[146:147], v[220:221]
	global_store_dwordx4 v117, v[218:221], s[46:47] nt
	v_cvt_f32_f16_e32 v112, v252
	v_cvt_f32_f16_sdwa v113, v252 dst_sel:DWORD dst_unused:UNUSED_PAD src0_sel:WORD_1
	v_cvt_f32_f16_e32 v114, v253
	v_cvt_f32_f16_sdwa v115, v253 dst_sel:DWORD dst_unused:UNUSED_PAD src0_sel:WORD_1
	v_add_u32_e32 v117, 0x69000, v163
	s_waitcnt lgkmcnt(1)
	v_pk_fma_f32 v[222:223], v[112:113], v[148:149], v[222:223]
	v_pk_fma_f32 v[224:225], v[114:115], v[150:151], v[224:225]
	global_store_dwordx4 v117, v[222:225], s[46:47] nt
	v_cvt_f32_f16_e32 v112, v254
	v_cvt_f32_f16_sdwa v113, v254 dst_sel:DWORD dst_unused:UNUSED_PAD src0_sel:WORD_1
	v_cvt_f32_f16_e32 v114, v255
	v_cvt_f32_f16_sdwa v115, v255 dst_sel:DWORD dst_unused:UNUSED_PAD src0_sel:WORD_1
	v_add_u32_e32 v117, 0x69000, v164
	s_waitcnt lgkmcnt(0)
	v_pk_fma_f32 v[226:227], v[112:113], v[152:153], v[226:227]
	v_pk_fma_f32 v[228:229], v[114:115], v[154:155], v[228:229]
	global_store_dwordx4 v117, v[226:229], s[46:47] nt
